# v6: diff-attn adds/q-DMA overlap, P0 adaLN 16-deep, moe_gu idx via LDS-DMA, router staging 16-deep, nt on read-once streams (mla_fin, df_finqk, df_fino, final) and out stores; no early-MFMA
# baseline (speedup 1.0000x reference)
; __device__ __forceinline__ void dq_load(DqRow& R, int m, const bf16* QKV, const float* cb, const float* sb, int u, int p) {
;     const bf16* s = QKV + (size_t)m * 3072 + u * 64;
;     R.q0 = *(const v4u*)(s + 8 * p); R.q1 = *(const v4u*)(s + 32 + 8 * p); R.k0 = *(const v4u*)(s + 1024 + 8 * p); R.k1 = *(const v4u*)(s + 1024 + 32 + 8 * p);
;     if (m < NLAT) { const int t = m & 4095; R.c0 = *(const f32x4*)(cb + t * 32 + 8 * p); R.c1 = *(const f32x4*)(cb + t * 32 + 8 * p + 4); R.s0 = *(const f32x4*)(sb + t * 32 + 8 * p); R.s1 = *(const f32x4*)(sb + t * 32 + 8 * p + 4); }
;     else { R.c0 = R.c1 = (f32x4){1.f, 1.f, 1.f, 1.f}; R.s0 = R.s1 = (f32x4){0.f, 0.f, 0.f, 0.f}; }
; }
; __device__ __forceinline__ void diff_finish_qk_phase(Frame& F, const InPtrs& A) {
;     const int gw = F.vcu * NWAVES + F.wave, NGW = F.G * NWAVES, lane = F.lane, u = lane >> 2, p = lane & 3;
;     const bf16* QKV = (const bf16*)(F.ws + R_QKV);
;     bf16* DQ = (bf16*)(F.ws + R_DQ); bf16* DQC = (bf16*)(F.ws + R_DQC); bf16* DK = (bf16*)(F.ws + R_DK);
;     const float* cb = (const float*)(F.ws + WS_ROPEB); const float* sb = cb + 4096 * 32;
;     float gq[16], gk[16];
;     { const float* qn = A[I_DF_QN]; const float* kn = A[I_DF_KN];
; #pragma unroll
;       for (int i = 0; i < 8; ++i) { gq[i] = qn[8 * p + i] * att::Sc<64>::C; gq[8 + i] = qn[32 + 8 * p + i] * att::Sc<64>::C; gk[i] = kn[8 * p + i]; gk[8 + i] = kn[32 + 8 * p + i]; } }
;     DqRow N;
;     if (gw < MROWS) dq_load(N, gw, QKV, cb, sb, u, p);
;     for (int m = gw; m < MROWS; m += NGW) {
;         const DqRow R = N;
;         { const int mn = m + NGW; if (mn < MROWS) dq_load(N, mn, QKV, cb, sb, u, p); }
.LBB0_757:
	s_andn2_b64 vcc, exec, s[0:1]
	s_cbranch_vccnz .LBB0_824
	v_readlane_b32 s0, v251, 12
	v_mbcnt_lo_u32_b32 v0, -1, 0
	v_mbcnt_hi_u32_b32 v0, -1, v0
	v_readlane_b32 s5, v251, 3
	v_readlane_b32 s2, v251, 2
	s_waitcnt vmcnt(0)
	v_add_u32_e32 v60, s0, v0
	s_nop 0
	v_readfirstlane_b32 s0, v60
	s_ashr_i32 s4, s0, 6
	s_mov_b64 s[0:1], 0
	s_lshl_b32 s5, s5, 3
	s_add_i32 s20, s5, s4
	v_readlane_b32 s4, v252, 1
	s_cmp_gt_i32 s20, 0x87ff
	s_nop 0
	v_mov_b32_e32 v0, s4
	ds_read_b32 v0, v0
	v_readlane_b32 s4, v252, 2
	s_waitcnt lgkmcnt(0)
	v_readfirstlane_b32 s6, v0
	v_mov_b32_e32 v0, s4
	ds_read_b32 v0, v0
	v_readlane_b32 s4, v252, 3
	s_waitcnt lgkmcnt(0)
	v_readfirstlane_b32 s7, v0
	v_mov_b32_e32 v0, s4
	ds_read_b32 v0, v0
	v_readlane_b32 s4, v252, 4
	s_waitcnt lgkmcnt(0)
	v_readfirstlane_b32 s8, v0
	v_mov_b32_e32 v0, s4
	ds_read_b32 v0, v0
	s_waitcnt lgkmcnt(0)
	v_readfirstlane_b32 s9, v0
	s_cbranch_scc1 .LBB0_768
	v_readlane_b32 s12, v251, 4
	v_readlane_b32 s14, v251, 6
	v_readlane_b32 s15, v251, 7
	s_add_u32 s4, s14, s0
	s_addc_u32 s5, s15, s1
	v_readlane_b32 s13, v251, 5
	s_add_u32 s12, s4, 0x280000
	v_lshlrev_b32_e32 v0, 3, v60
	s_addc_u32 s13, s5, 0
	v_and_b32_e32 v20, 24, v0
	s_add_u32 s14, s4, 0x300000
	v_lshlrev_b32_e32 v58, 2, v20
	s_addc_u32 s15, s5, 0
	global_load_dwordx4 v[46:49], v58, s[6:7] offset:16
	global_load_dwordx4 v[54:57], v58, s[6:7]
	global_load_dwordx4 v[42:45], v58, s[6:7] offset:144
	global_load_dwordx4 v[50:53], v58, s[6:7] offset:128
	global_load_dwordx4 v[2:5], v58, s[8:9] offset:16
	global_load_dwordx4 v[6:9], v58, s[8:9]
	global_load_dwordx4 v[10:13], v58, s[8:9] offset:144
	global_load_dwordx4 v[14:17], v58, s[8:9] offset:128
	s_mul_i32 s6, s20, 0x1800
	v_bfe_u32 v82, v60, 2, 4
	s_mul_hi_i32 s7, s20, 0x1800
	s_add_u32 s6, s4, s6
	s_addc_u32 s7, s5, s7
	v_lshlrev_b32_e32 v0, 7, v82
	v_lshl_add_u64 v[18:19], s[6:7], 0, v[0:1]
	v_lshlrev_b32_e32 v84, 1, v20
	v_mov_b32_e32 v85, v1
	v_lshl_add_u64 v[18:19], v[18:19], 0, v[84:85]
	s_mov_b64 s[6:7], 0xdc00000
	v_lshl_add_u64 v[20:21], v[18:19], 0, s[6:7]
	v_add_co_u32_e32 v18, vcc, 0xdc00000, v18
	s_cmpk_gt_i32 s20, 0x7fff
	s_nop 0
	v_addc_co_u32_e32 v19, vcc, 0, v19, vcc
	global_load_dwordx4 v[74:77], v[20:21], off offset:64 nt
	global_load_dwordx4 v[38:41], v[20:21], off offset:2048 nt
	global_load_dwordx4 v[78:81], v[18:19], off nt
	global_load_dwordx4 v[34:37], v[20:21], off offset:2112 nt
	s_cbranch_scc1 .LBB0_761
	s_lshl_b32 s6, s20, 7
	s_and_b32 s8, s6, 0x7ff80
	s_add_u32 s6, s12, s8
	s_addc_u32 s7, s13, 0
	global_load_dwordx4 v[18:21], v58, s[6:7]
	global_load_dwordx4 v[22:25], v58, s[6:7] offset:16
	s_add_u32 s6, s14, s8
	s_addc_u32 s7, s15, 0
	global_load_dwordx4 v[26:29], v58, s[6:7]
	global_load_dwordx4 v[30:33], v58, s[6:7] offset:16
	s_waitcnt vmcnt(3)
	v_mov_b32_e32 v86, v19
	v_mov_b32_e32 v19, v20
	v_mov_b32_e32 v87, v21
	s_waitcnt vmcnt(2)
	v_mov_b32_e32 v20, v23
	v_mov_b32_e32 v23, v24
	v_mov_b32_e32 v21, v25
	s_waitcnt vmcnt(1)
	v_mov_b32_e32 v90, v27
	v_mov_b32_e32 v27, v28
	v_mov_b32_e32 v91, v29
	s_waitcnt vmcnt(0)
	v_mov_b32_e32 v96, v31
	v_mov_b32_e32 v31, v32
	v_mov_b32_e32 v97, v33
	s_branch .LBB0_762

; __device__ __forceinline__ void dq_load(DqRow& R, int m, const bf16* QKV, const float* cb, const float* sb, int u, int p) {
;     const bf16* s = QKV + (size_t)m * 3072 + u * 64;
;     R.q0 = *(const v4u*)(s + 8 * p); R.q1 = *(const v4u*)(s + 32 + 8 * p); R.k0 = *(const v4u*)(s + 1024 + 8 * p); R.k1 = *(const v4u*)(s + 1024 + 32 + 8 * p);
;     if (m < NLAT) { const int t = m & 4095; R.c0 = *(const f32x4*)(cb + t * 32 + 8 * p); R.c1 = *(const f32x4*)(cb + t * 32 + 8 * p + 4); R.s0 = *(const f32x4*)(sb + t * 32 + 8 * p); R.s1 = *(const f32x4*)(sb + t * 32 + 8 * p + 4); }
;     else { R.c0 = R.c1 = (f32x4){1.f, 1.f, 1.f, 1.f}; R.s0 = R.s1 = (f32x4){0.f, 0.f, 0.f, 0.f}; }
; }
.LBB0_763:
	s_and_b32 s0, s17, 0x1ffe0
	s_lshl_b32 s2, s0, 2
	v_lshl_add_u64 v[62:63], v[28:29], 0, s[2:3]
	v_lshl_add_u64 v[64:65], v[24:25], 0, s[2:3]
	global_load_dwordx4 v[58:61], v[62:63], off offset:16 nt
	global_load_dwordx4 v[70:73], v[62:63], off nt
	global_load_dwordx4 v[66:69], v[64:65], off offset:16 nt
	s_nop 0
	global_load_dwordx4 v[62:65], v[64:65], off nt

; __device__ __forceinline__ void dq_load(DqRow& R, int m, const bf16* QKV, const float* cb, const float* sb, int u, int p) {
;     const bf16* s = QKV + (size_t)m * 3072 + u * 64;
;     R.q0 = *(const v4u*)(s + 8 * p); R.q1 = *(const v4u*)(s + 32 + 8 * p); R.k0 = *(const v4u*)(s + 1024 + 8 * p); R.k1 = *(const v4u*)(s + 1024 + 32 + 8 * p);
;     if (m < NLAT) { const int t = m & 4095; R.c0 = *(const f32x4*)(cb + t * 32 + 8 * p); R.c1 = *(const f32x4*)(cb + t * 32 + 8 * p + 4); R.s0 = *(const f32x4*)(sb + t * 32 + 8 * p); R.s1 = *(const f32x4*)(sb + t * 32 + 8 * p + 4); }
;     else { R.c0 = R.c1 = (f32x4){1.f, 1.f, 1.f, 1.f}; R.s0 = R.s1 = (f32x4){0.f, 0.f, 0.f, 0.f}; }
; }
; __device__ __forceinline__ void diff_finish_qk_phase(Frame& F, const InPtrs& A) {
;     const int gw = F.vcu * NWAVES + F.wave, NGW = F.G * NWAVES, lane = F.lane, u = lane >> 2, p = lane & 3;
;     const bf16* QKV = (const bf16*)(F.ws + R_QKV);
;     bf16* DQ = (bf16*)(F.ws + R_DQ); bf16* DQC = (bf16*)(F.ws + R_DQC); bf16* DK = (bf16*)(F.ws + R_DK);
;     const float* cb = (const float*)(F.ws + WS_ROPEB); const float* sb = cb + 4096 * 32;
;     float gq[16], gk[16];
;     { const float* qn = A[I_DF_QN]; const float* kn = A[I_DF_KN];
; #pragma unroll
;       for (int i = 0; i < 8; ++i) { gq[i] = qn[8 * p + i] * att::Sc<64>::C; gq[8 + i] = qn[32 + 8 * p + i] * att::Sc<64>::C; gk[i] = kn[8 * p + i]; gk[8 + i] = kn[32 + 8 * p + i]; } }
;     DqRow N;
;     if (gw < MROWS) dq_load(N, gw, QKV, cb, sb, u, p);
;     for (int m = gw; m < MROWS; m += NGW) {
;         const DqRow R = N;
;         { const int mn = m + NGW; if (mn < MROWS) dq_load(N, mn, QKV, cb, sb, u, p); }
.LBB0_765:
	s_add_i32 s19, s20, s16
	s_cmp_gt_i32 s19, 0x87ff
	s_cselect_b64 s[14:15], -1, 0
	s_and_b64 vcc, exec, s[14:15]
	v_mov_b32_e32 v66, v30
	v_mov_b32_e32 v67, v96
	v_mov_b32_e32 v68, v31
	v_mov_b32_e32 v69, v97
	v_mov_b32_e32 v62, v26
	v_mov_b32_e32 v63, v90
	v_mov_b32_e32 v64, v27
	v_mov_b32_e32 v65, v91
	v_mov_b32_e32 v58, v22
	v_mov_b32_e32 v59, v20
	v_mov_b32_e32 v60, v23
	v_mov_b32_e32 v61, v21
	v_mov_b32_e32 v70, v18
	v_mov_b32_e32 v71, v86
	v_mov_b32_e32 v72, v19
	v_mov_b32_e32 v73, v87
	s_cbranch_vccnz .LBB0_764
	global_load_dwordx4 v[54:57], v[112:113], off offset:-2048 nt
	global_load_dwordx4 v[50:53], v[112:113], off offset:-1984 nt
	global_load_dwordx4 v[46:49], v[112:113], off nt
	global_load_dwordx4 v[42:45], v[112:113], off offset:64 nt
	s_cmpk_gt_i32 s19, 0x7fff
	s_cbranch_scc0 .LBB0_763
	v_mov_b32_e32 v65, 0
	v_mov_b32_e32 v73, 1.0
	v_mov_b32_e32 v72, 1.0
	v_mov_b32_e32 v71, 1.0
	v_mov_b32_e32 v70, 1.0
	v_mov_b32_e32 v61, 1.0
	v_mov_b32_e32 v60, 1.0
	v_mov_b32_e32 v59, 1.0
	v_mov_b32_e32 v58, 1.0
	v_mov_b32_e32 v64, 0
	v_mov_b32_e32 v63, 0
	v_mov_b32_e32 v62, 0
	v_mov_b32_e32 v69, 0
	v_mov_b32_e32 v68, 0
	v_mov_b32_e32 v67, 0
	v_mov_b32_e32 v66, 0
	s_branch .LBB0_764

; __device__ __forceinline__ void diff_finish_o_phase(Frame& F, const InPtrs& A, float lam_init) {
;     const int gw = F.vcu * NWAVES + F.wave, NGW = F.G * NWAVES, lane = F.lane, h = lane >> 3, p = lane & 7;
;     const bf16* OB = (const bf16*)(F.ws + R_OB); bf16* AO = (bf16*)(F.ws + R_DAO);
;     const float d1 = wave_sum(A[I_DF_LQ1][lane] * A[I_DF_LK1][lane]), d2 = wave_sum(A[I_DF_LQ2][lane] * A[I_DF_LK2][lane]);
;     const float lam = expf(d1) - expf(d2) + lam_init, post = 1.0f - lam_init;
.LBB0_1027:
	s_andn2_b64 vcc, exec, s[0:1]
	s_cbranch_vccnz .LBB0_1089
	v_readlane_b32 s0, v251, 12
	v_mbcnt_lo_u32_b32 v0, -1, 0
	v_mbcnt_hi_u32_b32 v0, -1, v0
	v_readlane_b32 s5, v251, 3
	v_readlane_b32 s2, v251, 2
	s_waitcnt vmcnt(0)
	v_add_u32_e32 v54, s0, v0
	s_nop 0
	v_readfirstlane_b32 s0, v54
	s_ashr_i32 s4, s0, 6
	s_mov_b64 s[0:1], 0
	s_lshl_b32 s5, s5, 3
	s_add_i32 s4, s5, s4
	v_readlane_b32 s5, v252, 11
	v_and_b32_e32 v0, 63, v54
	s_waitcnt lgkmcnt(0)
	v_lshlrev_b32_e32 v4, 2, v0
	v_mov_b32_e32 v2, s5
	ds_read_b32 v2, v2
	v_readlane_b32 s5, v252, 12
	s_cmp_gt_i32 s4, 0x87ff
	s_waitcnt lgkmcnt(0)
	v_readfirstlane_b32 s6, v2
	v_mov_b32_e32 v2, s5
	ds_read_b32 v2, v2
	v_readlane_b32 s5, v252, 13
	s_waitcnt lgkmcnt(0)
	v_readfirstlane_b32 s7, v2
	v_mov_b32_e32 v3, s5
	v_readlane_b32 s5, v252, 14
	s_nop 2
	global_load_dword v2, v4, s[6:7]
	ds_read_b32 v3, v3
	s_waitcnt lgkmcnt(0)
	v_readfirstlane_b32 s6, v3
	v_mov_b32_e32 v3, s5
	ds_read_b32 v3, v3
	v_readlane_b32 s5, v252, 15
	s_waitcnt lgkmcnt(0)
	v_readfirstlane_b32 s7, v3
	s_nop 4
	global_load_dword v3, v4, s[6:7]
	s_waitcnt vmcnt(0)
	v_mul_f32_e32 v5, v2, v3
	ds_swizzle_b32 v5, v5 offset:swizzle(SWAP,1)
	s_waitcnt lgkmcnt(0)
	v_fmac_f32_e32 v5, v2, v3
	ds_swizzle_b32 v2, v5 offset:swizzle(SWAP,2)
	s_waitcnt lgkmcnt(0)
	v_add_f32_e32 v2, v5, v2
	v_mov_b32_e32 v5, s5
	ds_read_b32 v5, v5
	v_readlane_b32 s5, v252, 16
	ds_swizzle_b32 v3, v2 offset:swizzle(SWAP,4)
	s_waitcnt lgkmcnt(1)
	v_readfirstlane_b32 s6, v5
	v_mov_b32_e32 v5, s5
	ds_read_b32 v5, v5
	v_readlane_b32 s5, v252, 17
	s_waitcnt lgkmcnt(1)
	v_add_f32_e32 v2, v2, v3
	ds_swizzle_b32 v3, v2 offset:swizzle(SWAP,8)
	v_mov_b32_e32 v6, s5
	s_waitcnt lgkmcnt(1)
	v_readfirstlane_b32 s7, v5
	v_readlane_b32 s5, v252, 18
	s_waitcnt lgkmcnt(0)
	v_add_f32_e32 v2, v2, v3
	ds_swizzle_b32 v3, v2 offset:swizzle(SWAP,16)
	s_waitcnt lgkmcnt(0)
	v_add_f32_e32 v2, v2, v3
	global_load_dword v5, v4, s[6:7]
	ds_read_b32 v6, v6
	v_mov_b32_e32 v3, v2
	s_nop 1
	v_permlane32_swap_b32_e32 v2, v3
	s_waitcnt lgkmcnt(0)
	v_readfirstlane_b32 s6, v6
	v_mov_b32_e32 v6, s5
	ds_read_b32 v6, v6
	v_readlane_b32 s5, v252, 19
	s_waitcnt lgkmcnt(0)
	v_readfirstlane_b32 s7, v6
	s_nop 4
	global_load_dword v4, v4, s[6:7]
	s_waitcnt vmcnt(0)
	v_mul_f32_e32 v6, v5, v4
	ds_swizzle_b32 v6, v6 offset:swizzle(SWAP,1)
	s_waitcnt lgkmcnt(0)
	v_fmac_f32_e32 v6, v5, v4
	ds_swizzle_b32 v4, v6 offset:swizzle(SWAP,2)
	s_waitcnt lgkmcnt(0)
	v_add_f32_e32 v4, v6, v4
	ds_swizzle_b32 v5, v4 offset:swizzle(SWAP,4)
	v_mov_b32_e32 v6, s5
	ds_read_b32 v6, v6
	v_readlane_b32 s5, v252, 20
	s_waitcnt lgkmcnt(1)
	v_add_f32_e32 v4, v4, v5
	ds_swizzle_b32 v5, v4 offset:swizzle(SWAP,8)
	s_waitcnt lgkmcnt(1)
	v_readfirstlane_b32 s6, v6
	v_mov_b32_e32 v6, s5
	ds_read_b32 v6, v6
	s_waitcnt lgkmcnt(1)
	v_add_f32_e32 v4, v4, v5
	ds_swizzle_b32 v5, v4 offset:swizzle(SWAP,16)
	s_waitcnt lgkmcnt(1)
	v_readfirstlane_b32 s7, v6
	s_waitcnt lgkmcnt(0)
	v_add_f32_e32 v4, v4, v5
	v_mov_b32_e32 v5, v4
	s_nop 1
	v_permlane32_swap_b32_e32 v4, v5
	s_cbranch_scc1 .LBB0_1033
; __device__ __forceinline__ void diff_finish_o_phase(Frame& F, const InPtrs& A, float lam_init) {
;     const int gw = F.vcu * NWAVES + F.wave, NGW = F.G * NWAVES, lane = F.lane, h = lane >> 3, p = lane & 7;
;     const bf16* OB = (const bf16*)(F.ws + R_OB); bf16* AO = (bf16*)(F.ws + R_DAO);
;     const float d1 = wave_sum(A[I_DF_LQ1][lane] * A[I_DF_LK1][lane]), d2 = wave_sum(A[I_DF_LQ2][lane] * A[I_DF_LK2][lane]);
;     const float lam = expf(d1) - expf(d2) + lam_init, post = 1.0f - lam_init;
;     float g[16];
;     { const float* sg = A[I_DF_SUBG];
; #pragma unroll
;       for (int i = 0; i < 16; ++i) g[i] = sg[16 * p + i] * post; }
;     v4u n0 = (v4u){0u, 0u, 0u, 0u}, n1 = n0, n2 = n0, n3 = n0;
;     if (gw < MROWS) { const bf16* s0 = OB + (size_t)gw * 2048 + (2 * h) * 128 + 16 * p; n0 = ((const v4u*)s0)[0]; n1 = ((const v4u*)s0)[1]; n2 = ((const v4u*)(s0 + 128))[0]; n3 = ((const v4u*)(s0 + 128))[1]; }
	v_lshlrev_b32_e32 v6, 4, v0
	v_and_b32_e32 v6, 0x70, v6
	v_lshlrev_b32_e32 v7, 2, v6
	global_load_dwordx4 v[30:33], v7, s[6:7]
	global_load_dwordx4 v[26:29], v7, s[6:7] offset:16
	global_load_dwordx4 v[22:25], v7, s[6:7] offset:32
	global_load_dwordx4 v[18:21], v7, s[6:7] offset:48
	v_readlane_b32 s12, v251, 4
	v_readlane_b32 s14, v251, 6
	v_readlane_b32 s15, v251, 7
	s_add_u32 s7, s14, s0
	v_readlane_b32 s8, v252, 32
	v_readlane_b32 s9, v252, 33
	s_addc_u32 s12, s15, s1
	s_ashr_i32 s5, s4, 31
	v_cvt_f32_u32_e32 v34, s8
	v_add_f32_e32 v50, v2, v3
	s_lshl_b32 s6, s2, 3
	s_lshl_b64 s[8:9], s[4:5], 12
	v_readlane_b32 s13, v251, 5
	v_lshrrev_b32_e32 v0, 3, v0
	v_mul_f32_e32 v2, 0x3fb8aa3b, v50
	s_add_u32 s8, s7, s8
	v_lshlrev_b32_e32 v52, 8, v0
	v_lshlrev_b32_e32 v0, 9, v0
	s_mov_b32 s13, 0x3fb8aa3b
	v_rndne_f32_e32 v3, v2
	s_addc_u32 s9, s12, s9
	v_fma_f32 v36, v50, s13, -v2
	v_sub_f32_e32 v38, v2, v3
	v_cvt_i32_f32_e32 v39, v3
	v_lshl_add_u64 v[2:3], s[8:9], 0, v[0:1]
	v_lshlrev_b32_e32 v0, 1, v6
	v_lshl_add_u64 v[2:3], v[2:3], 0, v[0:1]
	s_mov_b64 s[8:9], 0x23000000
	s_mov_b32 s2, 0x23000000
	v_lshl_add_u64 v[10:11], v[2:3], 0, s[8:9]
	v_add_co_u32_e32 v2, vcc, s2, v2
	v_add_f32_e32 v51, v4, v5
	s_nop 0
	v_addc_co_u32_e32 v3, vcc, 0, v3, vcc
	global_load_dwordx4 v[14:17], v[2:3], off nt
	s_nop 0
	global_load_dwordx4 v[2:5], v[10:11], off offset:272 nt
	global_load_dwordx4 v[6:9], v[10:11], off offset:16 nt
	s_nop 0
	global_load_dwordx4 v[10:13], v[10:11], off offset:256 nt
	v_mul_f32_e32 v35, 0x3fb8aa3b, v51
	v_rndne_f32_e32 v55, v35
	v_fmac_f32_e32 v36, 0x32a5705f, v50
	v_mul_f32_e32 v34, 0xbe99999a, v34
	v_fma_f32 v37, v51, s13, -v35
	v_sub_f32_e32 v0, v35, v55
	v_add_f32_e32 v35, v38, v36
	v_mul_f32_e32 v36, 0x3fb8aa3b, v34
	v_fma_f32 v38, v34, s13, -v36
	v_rndne_f32_e32 v40, v36
	v_fmac_f32_e32 v38, 0x32a5705f, v34
	v_sub_f32_e32 v36, v36, v40
	v_add_f32_e32 v36, v36, v38
	v_cvt_i32_f32_e32 v40, v40
	v_exp_f32_e32 v36, v36
	v_fmac_f32_e32 v37, 0x32a5705f, v51
	v_add_f32_e32 v0, v0, v37
	s_mov_b32 s2, 0xc2ce8ed0
	v_exp_f32_e32 v35, v35
	v_exp_f32_e32 v56, v0
	v_ldexp_f32 v0, v36, v40
	v_cmp_ngt_f32_e32 vcc, s2, v34
	s_mov_b32 s7, 0x42b17218
	v_ldexp_f32 v57, v35, v39
	v_cndmask_b32_e32 v0, 0, v0, vcc
	v_cmp_nlt_f32_e32 vcc, s7, v34
	v_mov_b32_e32 v34, 0x3f4ccccd
	s_lshl_b64 s[8:9], s[4:5], 11
	v_cndmask_b32_e32 v0, v248, v0, vcc
	v_fmamk_f32 v58, v0, 0xbf19999a, v34
	v_sub_f32_e32 v0, 1.0, v58
	v_cmp_ngt_f32_e32 vcc, s2, v50
	v_mov_b32_e32 v53, v1
	s_waitcnt vmcnt(7)
	v_mov_b32_e32 v34, v30
	v_mov_b32_e32 v35, v32
	v_mov_b32_e32 v32, v31
	s_waitcnt vmcnt(6)
	v_mov_b32_e32 v30, v26
	v_mov_b32_e32 v31, v28
	v_mov_b32_e32 v28, v27
	s_waitcnt vmcnt(5)
	v_mov_b32_e32 v26, v22
	v_mov_b32_e32 v27, v24
	v_mov_b32_e32 v24, v23
	s_waitcnt vmcnt(4)
	v_mov_b32_e32 v22, v18
	v_mov_b32_e32 v23, v20
	v_mov_b32_e32 v20, v19
	v_pk_mul_f32 v[34:35], v[0:1], v[34:35] op_sel_hi:[0,1]
	v_pk_mul_f32 v[36:37], v[0:1], v[32:33] op_sel_hi:[0,1]
	v_pk_mul_f32 v[38:39], v[0:1], v[30:31] op_sel_hi:[0,1]
	v_pk_mul_f32 v[40:41], v[0:1], v[28:29] op_sel_hi:[0,1]
	v_pk_mul_f32 v[42:43], v[0:1], v[26:27] op_sel_hi:[0,1]
	v_pk_mul_f32 v[44:45], v[0:1], v[24:25] op_sel_hi:[0,1]
	v_pk_mul_f32 v[46:47], v[0:1], v[22:23] op_sel_hi:[0,1]
	v_pk_mul_f32 v[48:49], v[0:1], v[20:21] op_sel_hi:[0,1]
	v_cvt_i32_f32_e32 v0, v55
	v_cndmask_b32_e32 v18, 0, v57, vcc
	v_cmp_nlt_f32_e32 vcc, s7, v50
	v_mov_b32_e32 v19, v1
	v_ldexp_f32 v0, v56, v0
	v_cndmask_b32_e32 v18, v248, v18, vcc
	v_cmp_ngt_f32_e32 vcc, s2, v51
	s_add_u32 s2, s0, s8
	s_addc_u32 s5, s1, s9
	s_add_u32 s8, s14, s2
	s_addc_u32 s9, s15, s5
	s_add_i32 s12, s4, s6
	v_cndmask_b32_e32 v0, 0, v0, vcc
	v_cmp_nlt_f32_e32 vcc, s7, v51
	s_ashr_i32 s7, s6, 31
	s_ashr_i32 s13, s12, 31
	v_lshl_add_u64 v[52:53], s[8:9], 0, v[52:53]
	s_lshl_b64 s[8:9], s[6:7], 11
	s_lshl_b64 s[12:13], s[12:13], 12
	s_add_u32 s0, s0, s12
	v_cndmask_b32_e32 v0, v248, v0, vcc
	s_addc_u32 s1, s1, s13
	v_readlane_b32 s2, v253, 25
	v_sub_f32_e32 v0, v18, v0
	v_lshlrev_b32_e32 v18, 6, v54
	s_add_u32 s0, s2, s0
	v_readlane_b32 s2, v253, 26
	v_and_b32_e32 v18, 0xe00, v18
	s_addc_u32 s1, s2, s1
	v_add_f32_e32 v50, v58, v0
	v_and_b32_e32 v0, 7, v54
	v_lshl_add_u64 v[54:55], s[0:1], 0, v[18:19]
	s_waitcnt vmcnt(2)
	v_mov_b64_e32 v[28:29], v[4:5]
	s_waitcnt vmcnt(0)
	v_mov_b64_e32 v[32:33], v[12:13]
	v_mov_b64_e32 v[20:21], v[8:9]
	v_mov_b64_e32 v[24:25], v[16:17]
	v_mov_b32_e32 v51, v50
	v_lshlrev_b32_e32 v0, 5, v0
	s_lshl_b64 s[12:13], s[6:7], 12
	v_mov_b64_e32 v[26:27], v[2:3]
	v_mov_b64_e32 v[30:31], v[10:11]
	v_mov_b64_e32 v[18:19], v[6:7]
	v_mov_b64_e32 v[22:23], v[14:15]
	s_branch .LBB0_1031

; __device__ __forceinline__ void diff_finish_o_phase(Frame& F, const InPtrs& A, float lam_init) {
;     ...
;     for (int m = gw; m < MROWS; m += NGW) {
;         const v4u c0 = n0, c1 = n1, c2 = n2, c3 = n3;
;         { const int mn = m + NGW; if (mn < MROWS) { const bf16* s0 = OB + (size_t)mn * 2048 + (2 * h) * 128 + 16 * p; n0 = ((const v4u*)s0)[0]; n1 = ((const v4u*)s0)[1]; n2 = ((const v4u*)(s0 + 128))[0]; n3 = ((const v4u*)(s0 + 128))[1]; } }
.LBB0_1031:
	s_add_i32 s4, s4, s6
	s_cmp_gt_i32 s4, 0x87ff
	s_cselect_b64 s[14:15], -1, 0
	s_and_b64 vcc, exec, s[14:15]
	s_cbranch_vccnz .LBB0_1030
	v_lshl_add_u64 v[30:31], v[54:55], 0, v[0:1]
	global_load_dwordx4 v[18:21], v[30:31], off offset:-240 nt
	global_load_dwordx4 v[22:25], v[30:31], off offset:-256 nt
	global_load_dwordx4 v[26:29], v[30:31], off offset:16 nt
	s_nop 0
	global_load_dwordx4 v[30:33], v[30:31], off nt
	s_branch .LBB0_1030

; __device__ __forceinline__ bf16* xb_row(const Frame& F, int row) { return (bf16*)(F.ws + WS_XB) + (size_t)row * D; }
; __device__ __forceinline__ void final_phase(Frame& F, int layer) {
;     const int gw = F.vcu * NWAVES + F.wave, NGW = F.G * NWAVES, lane = F.lane;
;     const float* MOD = (const float*)(F.ws + WS_MOD);
;     const bf16* YB = (const bf16*)(F.ws + R_YB); const int* SLOT = (const int*)(F.ws + WS_SLOT);
;     v2u vn[4]; int sln = -1;
;     if (gw < NLAT) { const bf16* src = xb_row(F, gw);
; #pragma unroll
;         for (int j = 0; j < 4; ++j) vn[j] = *(const v2u*)(src + 4 * (64 * j + lane));
;         sln = SLOT[(size_t)gw * 16 + (lane & 15)]; }
.LBB0_2074:
	v_readlane_b32 s2, v251, 10
	v_readlane_b32 s3, v251, 11
	s_cmp_ge_i32 s44, s2
	s_cselect_b64 s[0:1], -1, 0
	s_cmp_lt_i32 s44, s3
	s_cselect_b64 s[2:3], -1, 0
	s_and_b64 s[0:1], s[0:1], s[2:3]
	s_and_b64 vcc, exec, s[0:1]
	s_cbranch_vccz .LBB0_2162
	v_mbcnt_lo_u32_b32 v0, -1, 0
	v_mbcnt_hi_u32_b32 v0, -1, v0
	v_readlane_b32 s0, v251, 12
	v_readlane_b32 s8, v251, 4
	s_mov_b64 s[2:3], 0
	v_add_u32_e32 v0, s0, v0
	v_readlane_b32 s12, v251, 2
	v_readfirstlane_b32 s0, v0
	s_ashr_i32 s4, s0, 6
	v_readlane_b32 s5, v251, 3
	v_readlane_b32 s10, v251, 6
	v_readlane_b32 s11, v251, 7
	s_add_u32 s0, s10, s2
	s_addc_u32 s1, s11, s3
	s_lshl_b32 s5, s5, 3
	s_add_i32 s4, s5, s4
	s_add_u32 s6, s0, 0xd700000
	s_addc_u32 s7, s1, 0
	s_cmp_lt_i32 s4, 0x8000
	v_lshlrev_b32_e32 v1, 2, v0
	v_readlane_b32 s9, v251, 5
	s_cselect_b64 s[10:11], -1, 0
	v_and_b32_e32 v1, 0xfc, v1
	v_and_b32_e32 v0, 15, v0
	s_add_u32 s8, s0, 0x35c00000
	v_mov_b32_e32 v42, 0
	s_addc_u32 s9, s1, 0
	v_mov_b32_e32 v79, -1
	s_and_b64 vcc, exec, s[10:11]
	s_waitcnt vmcnt(0) lgkmcnt(0)
	v_lshlrev_b32_e32 v4, 2, v0
	v_lshlrev_b32_e32 v2, 1, v1
	v_mov_b32_e32 v43, 0
	v_mov_b32_e32 v32, 0
	v_mov_b32_e32 v33, 0
	v_mov_b32_e32 v22, 0
	v_mov_b32_e32 v23, 0
	v_mov_b32_e32 v18, 0
	v_mov_b32_e32 v19, 0
	s_cbranch_vccz .LBB0_2077
	s_ashr_i32 s5, s4, 31
	s_lshl_b64 s[14:15], s[4:5], 6
	s_add_u32 s14, s6, s14
	s_addc_u32 s15, s7, s15
	s_lshl_b64 s[16:17], s[4:5], 11
	s_add_u32 s16, s8, s16
	s_addc_u32 s17, s9, s17
	global_load_dwordx2 v[42:43], v2, s[16:17] nt
	global_load_dwordx2 v[32:33], v2, s[16:17] offset:512 nt
	global_load_dwordx2 v[22:23], v2, s[16:17] offset:1024 nt
	global_load_dwordx2 v[18:19], v2, s[16:17] offset:1536 nt
	global_load_dword v79, v4, s[14:15]

; __device__ __forceinline__ bf16* xb_row(const Frame& F, int row) { return (bf16*)(F.ws + WS_XB) + (size_t)row * D; }
; __device__ __forceinline__ void final_phase(Frame& F, int layer) {
;     ...
;     for (int m = gw; m < NLAT; m += NGW) {
;         float* xr = F.out + (size_t)m * D; const int rr = m >> 12;
;         f32x4 v[4]; const int sl = sln;
; #pragma unroll
;         for (int j = 0; j < 4; ++j) v[j] = (f32x4){bflo(vn[j].x), bfhi(vn[j].x), bflo(vn[j].y), bfhi(vn[j].y)};
;         { const int mn = m + NGW; if (mn < NLAT) { const bf16* src = xb_row(F, mn);
; #pragma unroll
;             for (int j = 0; j < 4; ++j) vn[j] = *(const v2u*)(src + 4 * (64 * j + lane));
;             sln = SLOT[(size_t)mn * 16 + (lane & 15)]; } }
;         f32x4 acc[4];
; #pragma unroll
;         for (int j = 0; j < 4; ++j) acc[j] = (f32x4){0.f, 0.f, 0.f, 0.f};
;         unsigned msk = (unsigned)(__ballot(sl >= 0) & 0xffffull);
;         while (msk) {
;             int sidx[4]; v2u w[4][4];
; #pragma unroll
;             for (int q = 0; q < 4; ++q) { sidx[q] = -1; if (msk) { const int e = __builtin_ctz(msk); msk &= msk - 1u; sidx[q] = __builtin_amdgcn_readlane(sl, e); } }
; #pragma unroll
;             for (int q = 0; q < 4; ++q) if (sidx[q] >= 0) { const bf16* y = YB + (size_t)sidx[q] * 1024;
; #pragma unroll
;                 for (int j = 0; j < 4; ++j) w[q][j] = *(const v2u*)(y + 4 * (64 * j + lane)); }
; #pragma unroll
;             for (int q = 0; q < 4; ++q) if (sidx[q] >= 0) {
; #pragma unroll
;                 for (int j = 0; j < 4; ++j) acc[j] += (f32x4){bflo(w[q][j].x), bfhi(w[q][j].x), bflo(w[q][j].y), bfhi(w[q][j].y)}; }
;         }
;         const float* g2 = MOD + ((size_t)layer * 9 + rr) * 6144 + 5120;
; #pragma unroll
;         for (int j = 0; j < 4; ++j) *(f32x4*)(xr + 4 * (64 * j + lane)) = v[j] + *(const f32x4*)(g2 + 4 * (64 * j + lane)) * acc[j];
.LBB0_2079:
	s_ashr_i32 s2, s4, 12
	s_ashr_i32 s5, s4, 31
	s_add_i32 s2, s2, 27
	s_lshl_b64 s[10:11], s[4:5], 12
	s_mul_hi_i32 s4, s2, 0x6000
	s_mulk_i32 s2, 0x6000
	s_add_u32 s2, s0, s2
	s_addc_u32 s5, s1, s4
	s_add_u32 s4, s2, 0x105000
	s_addc_u32 s5, s5, 0
	global_load_dwordx4 v[80:83], v28, s[4:5]
	v_lshlrev_b32_e32 v84, 16, v42
	v_and_b32_e32 v85, 0xffff0000, v42
	v_lshlrev_b32_e32 v42, 16, v43
	v_and_b32_e32 v43, 0xffff0000, v43
	v_lshl_add_u64 v[86:87], v[30:31], 0, s[10:11]
	s_waitcnt vmcnt(1)
	v_mov_b32_e32 v79, v78
	s_andn2_b64 vcc, exec, s[8:9]
	s_waitcnt vmcnt(0)
	v_pk_fma_f32 v[2:3], v[2:3], v[80:81], v[84:85]
	v_pk_fma_f32 v[4:5], v[4:5], v[82:83], v[42:43]
	global_store_dwordx4 v[86:87], v[2:5], off nt
	global_load_dwordx4 v[2:5], v29, s[4:5]
	v_lshlrev_b32_e32 v42, 16, v32
	v_and_b32_e32 v43, 0xffff0000, v32
	v_lshlrev_b32_e32 v32, 16, v33
	v_and_b32_e32 v33, 0xffff0000, v33
	s_waitcnt vmcnt(0)
	v_pk_fma_f32 v[2:3], v[6:7], v[2:3], v[42:43]
	v_pk_fma_f32 v[4:5], v[8:9], v[4:5], v[32:33]
	global_store_dwordx4 v[86:87], v[2:5], off offset:1024 nt
	global_load_dwordx4 v[2:5], v76, s[4:5]
	v_lshlrev_b32_e32 v6, 16, v22
	v_and_b32_e32 v7, 0xffff0000, v22
	v_lshlrev_b32_e32 v8, 16, v23
	v_and_b32_e32 v9, 0xffff0000, v23
	v_mov_b32_e32 v42, v70
	v_mov_b32_e32 v43, v71
	v_mov_b32_e32 v32, v72
	v_mov_b32_e32 v33, v73
	v_mov_b32_e32 v22, v74
	v_mov_b32_e32 v23, v75
	s_waitcnt vmcnt(0)
	v_pk_fma_f32 v[2:3], v[10:11], v[2:3], v[6:7]
	v_pk_fma_f32 v[4:5], v[12:13], v[4:5], v[8:9]
	global_store_dwordx4 v[86:87], v[2:5], off offset:2048 nt
	global_load_dwordx4 v[2:5], v77, s[4:5]
	v_lshlrev_b32_e32 v6, 16, v18
	v_and_b32_e32 v7, 0xffff0000, v18
	v_lshlrev_b32_e32 v8, 16, v19
	v_and_b32_e32 v9, 0xffff0000, v19
	v_mov_b32_e32 v18, v68
	s_mov_b32 s4, s6
	v_mov_b32_e32 v19, v69
	s_waitcnt vmcnt(0)
	v_pk_fma_f32 v[2:3], v[14:15], v[2:3], v[6:7]
	v_pk_fma_f32 v[4:5], v[16:17], v[4:5], v[8:9]
	global_store_dwordx4 v[86:87], v[2:5], off offset:3072 nt
	s_cbranch_vccz .LBB0_2106
.LBB0_2080:
	s_add_i32 s6, s4, s20
	s_cmpk_gt_i32 s6, 0x7fff
	s_cselect_b64 s[8:9], -1, 0
	s_and_b64 vcc, exec, s[8:9]
	v_mov_b32_e32 v70, v42
	v_mov_b32_e32 v71, v43
	v_mov_b32_e32 v72, v32
	v_mov_b32_e32 v73, v33
	v_mov_b32_e32 v74, v22
	v_mov_b32_e32 v75, v23
	v_mov_b32_e32 v68, v18
	v_mov_b32_e32 v69, v19
	s_cbranch_vccnz .LBB0_2082
	s_ashr_i32 s7, s6, 31
	s_lshl_b64 s[10:11], s[6:7], 11
	v_lshl_add_u64 v[2:3], v[24:25], 0, s[10:11]
	global_load_dwordx2 v[70:71], v[2:3], off nt
	global_load_dwordx2 v[72:73], v[2:3], off offset:512 nt
	global_load_dwordx2 v[74:75], v[2:3], off offset:1024 nt
	global_load_dwordx2 v[68:69], v[2:3], off offset:1536 nt
	s_lshl_b64 s[10:11], s[6:7], 6
	v_lshl_add_u64 v[2:3], v[20:21], 0, s[10:11]
	global_load_dword v78, v[2:3], off

; __device__ __forceinline__ void final_phase(Frame& F, int layer) {
;     ...
;         unsigned msk = (unsigned)(__ballot(sl >= 0) & 0xffffull);
;         while (msk) {
;             int sidx[4]; v2u w[4][4];
; #pragma unroll
;             for (int q = 0; q < 4; ++q) { sidx[q] = -1; if (msk) { const int e = __builtin_ctz(msk); msk &= msk - 1u; sidx[q] = __builtin_amdgcn_readlane(sl, e); } }
; #pragma unroll
;             for (int q = 0; q < 4; ++q) if (sidx[q] >= 0) { const bf16* y = YB + (size_t)sidx[q] * 1024;
; #pragma unroll
;                 for (int j = 0; j < 4; ++j) w[q][j] = *(const v2u*)(y + 4 * (64 * j + lane)); }
; #pragma unroll
;             for (int q = 0; q < 4; ++q) if (sidx[q] >= 0) {
; #pragma unroll
;                 for (int j = 0; j < 4; ++j) acc[j] += (f32x4){bflo(w[q][j].x), bfhi(w[q][j].x), bflo(w[q][j].y), bfhi(w[q][j].y)}; }
.LBB0_2090:
	s_lshl_b64 s[14:15], s[2:3], 11
	s_waitcnt vmcnt(0)
	v_lshl_add_u64 v[60:61], v[26:27], 0, s[14:15]
	global_load_dwordx2 v[66:67], v[60:61], off nt
	global_load_dwordx2 v[64:65], v[60:61], off offset:512 nt
	global_load_dwordx2 v[62:63], v[60:61], off offset:1024 nt
	s_nop 0
	global_load_dwordx2 v[60:61], v[60:61], off offset:1536 nt
.LBB0_2091:
	s_cmp_gt_i32 s12, -1
	s_cselect_b64 s[14:15], -1, 0
	s_cmp_lt_i32 s12, 0
	s_cbranch_scc1 .LBB0_2093
	s_mov_b32 s13, s3
	s_lshl_b64 s[12:13], s[12:13], 11
	s_waitcnt vmcnt(0)
	v_lshl_add_u64 v[52:53], v[26:27], 0, s[12:13]
	global_load_dwordx2 v[58:59], v[52:53], off nt
	global_load_dwordx2 v[56:57], v[52:53], off offset:512 nt
	global_load_dwordx2 v[54:55], v[52:53], off offset:1024 nt
	s_nop 0
	global_load_dwordx2 v[52:53], v[52:53], off offset:1536 nt
.LBB0_2093:
	s_cmp_gt_i32 s10, -1
	s_cselect_b64 s[12:13], -1, 0
	s_cmp_lt_i32 s10, 0
	s_cbranch_scc1 .LBB0_2095
	s_mov_b32 s11, s3
	s_lshl_b64 s[10:11], s[10:11], 11
	s_waitcnt vmcnt(0)
	v_lshl_add_u64 v[44:45], v[26:27], 0, s[10:11]
	global_load_dwordx2 v[50:51], v[44:45], off nt
	global_load_dwordx2 v[48:49], v[44:45], off offset:512 nt
	global_load_dwordx2 v[46:47], v[44:45], off offset:1024 nt
	s_nop 0
	global_load_dwordx2 v[44:45], v[44:45], off offset:1536 nt
.LBB0_2095:
	s_cmp_gt_i32 s18, -1
	s_cselect_b64 s[10:11], -1, 0
	s_cmp_lt_i32 s18, 0
	s_cbranch_scc1 .LBB0_2097
	s_mov_b32 s19, s3
	s_lshl_b64 s[18:19], s[18:19], 11
	s_waitcnt vmcnt(0)
	v_lshl_add_u64 v[34:35], v[26:27], 0, s[18:19]
	global_load_dwordx2 v[40:41], v[34:35], off nt
	global_load_dwordx2 v[38:39], v[34:35], off offset:512 nt
	global_load_dwordx2 v[36:37], v[34:35], off offset:1024 nt
	s_nop 0
	global_load_dwordx2 v[34:35], v[34:35], off offset:1536 nt
